# baseline (speedup 1.0000x reference)
_Z12final_kernelPKfPKiPK15HIP_vector_typeIiLj4EES2_S2_S0_S0_S0_S0_Pf:
	s_load_dwordx2 s[4:5], s[0:1], 0x10
	s_ashr_i32 s3, s2, 31
	s_lshl_b64 s[6:7], s[2:3], 4
	s_waitcnt lgkmcnt(0)
	s_add_u32 s4, s4, s6
	s_addc_u32 s5, s5, s7
	s_load_dwordx4 s[4:7], s[4:5], 0x0
	s_waitcnt lgkmcnt(0)
	s_cmp_eq_u32 s6, 0
	s_cbranch_scc1 .LBB4_17
	s_load_dwordx2 s[12:13], s[0:1], 0x8
	s_load_dwordx2 s[18:19], s[0:1], 0x0
	s_load_dwordx4 s[8:11], s[0:1], 0x20
	s_load_dwordx2 s[16:17], s[0:1], 0x30
	s_load_dwordx4 s[36:39], s[0:1], 0x38
	s_load_dwordx2 s[40:41], s[0:1], 0x48
	s_movk_i32 s20, 0x51f
	s_add_i32 s21, s6, -1
	s_movk_i32 s34, 0x5556
	s_movk_i32 s35, 0x64
	v_add_u32_e32 v1, 0x100, v0
	v_add_u32_e32 v2, 0x200, v0
	v_add_u32_e32 v3, 0x300, v0
	v_min_u32_e32 v3, 0x31f, v3
	v_mul_u32_u24_e32 v4, s20, v0
	v_mul_u32_u24_e32 v5, s20, v1
	v_mul_u32_u24_e32 v6, s20, v2
	v_mul_u32_u24_e32 v7, s20, v3
	v_lshrrev_b32_e32 v4, 15, v4
	v_lshrrev_b32_e32 v5, 15, v5
	v_lshrrev_b32_e32 v6, 15, v6
	v_lshrrev_b32_e32 v7, 15, v7
	v_mul_u32_u24_e32 v8, 25, v4
	v_mul_u32_u24_e32 v9, 25, v5
	v_mul_u32_u24_e32 v10, 25, v6
	v_mul_u32_u24_e32 v11, 25, v7
	v_sub_u32_e32 v8, v0, v8
	v_sub_u32_e32 v9, v1, v9
	v_sub_u32_e32 v10, v2, v10
	v_sub_u32_e32 v11, v3, v11
	v_min_u32_e32 v12, s21, v4
	v_min_u32_e32 v13, s21, v5
	v_min_u32_e32 v14, s21, v6
	v_min_u32_e32 v15, s21, v7
	v_add_lshl_u32 v12, v12, s5, 2
	v_add_lshl_u32 v13, v13, s5, 2
	v_add_lshl_u32 v14, v14, s5, 2
	v_add_lshl_u32 v15, v15, s5, 2
	v_mul_u32_u24_e32 v130, s34, v0
	v_lshrrev_b32_e32 v130, 16, v130
	v_mul_u32_u24_e32 v131, 3, v130
	v_sub_u32_e32 v131, v0, v131
	v_min_u32_e32 v132, s21, v130
	v_add_lshl_u32 v132, v132, s5, 2
	v_lshlrev_b32_e32 v133, 2, v131
	v_min_u32_e32 v134, 0x4a, v0
	v_lshlrev_b32_e32 v134, 4, v134
	s_waitcnt lgkmcnt(0)
	s_mul_i32 s22, s4, 0x4b0
	s_add_u32 s36, s36, s22
	s_addc_u32 s37, s37, 0
	s_mul_i32 s22, s4, 12
	s_add_u32 s38, s38, s22
	s_addc_u32 s39, s39, 0
	global_load_dwordx4 v[124:127], v134, s[36:37]
	global_load_dword v128, v133, s[38:39]
	global_load_dword v129, v132, s[12:13]
	global_load_dword v12, v12, s[12:13]
	global_load_dword v13, v13, s[12:13]
	global_load_dword v14, v14, s[12:13]
	global_load_dword v15, v15, s[12:13]
	s_mul_i32 s22, s2, 0xc800
	s_add_u32 s24, s18, s22
	s_addc_u32 s25, s19, 0
	s_add_u32 s26, s24, 0x3200
	s_addc_u32 s27, s25, 0
	s_add_u32 s28, s24, 0x6400
	s_addc_u32 s29, s25, 0
	s_add_u32 s30, s24, 0x9600
	s_addc_u32 s31, s25, 0
	s_mul_i32 s22, s4, 0x190
	s_add_u32 s16, s16, s22
	s_addc_u32 s17, s17, 0
	s_mul_i32 s32, s4, 0x864
	s_addk_i32 s32, 0x800
	s_movk_i32 s33, 0x190
	v_lshlrev_b32_e32 v112, 4, v0
	v_lshlrev_b32_e32 v113, 4, v1
	v_lshlrev_b32_e32 v114, 4, v2
	v_lshlrev_b32_e32 v115, 4, v3
	v_lshlrev_b32_e32 v116, 4, v8
	v_lshlrev_b32_e32 v117, 4, v9
	v_lshlrev_b32_e32 v118, 4, v10
	v_lshlrev_b32_e32 v119, 4, v11
	v_lshlrev_b32_e32 v135, 2, v0
	v_add_u32_e32 v136, 0, v135
	v_mul_u32_u24_e32 v137, s34, v136
	v_lshrrev_b32_e32 v137, 16, v137
	v_mul_u32_u24_e32 v138, 3, v137
	v_sub_u32_e32 v138, v136, v138
	v_mad_u32_u24 v138, v138, s35, v137
	v_lshlrev_b32_e32 v4, 2, v138
	v_add_u32_e32 v136, 1, v135
	v_mul_u32_u24_e32 v137, s34, v136
	v_lshrrev_b32_e32 v137, 16, v137
	v_mul_u32_u24_e32 v138, 3, v137
	v_sub_u32_e32 v138, v136, v138
	v_mad_u32_u24 v138, v138, s35, v137
	v_lshlrev_b32_e32 v5, 2, v138
	v_add_u32_e32 v136, 2, v135
	v_mul_u32_u24_e32 v137, s34, v136
	v_lshrrev_b32_e32 v137, 16, v137
	v_mul_u32_u24_e32 v138, 3, v137
	v_sub_u32_e32 v138, v136, v138
	v_mad_u32_u24 v138, v138, s35, v137
	v_lshlrev_b32_e32 v6, 2, v138
	v_add_u32_e32 v136, 3, v135
	v_mul_u32_u24_e32 v137, s34, v136
	v_lshrrev_b32_e32 v137, 16, v137
	v_mul_u32_u24_e32 v138, 3, v137
	v_sub_u32_e32 v138, v136, v138
	v_mad_u32_u24 v138, v138, s35, v137
	v_lshlrev_b32_e32 v7, 2, v138
	s_waitcnt vmcnt(0)
	v_cmp_gt_u32_e32 vcc, 0x4b, v0
	s_and_saveexec_b64 s[14:15], vcc
	ds_write_b32 v4, v124 offset:12800
	ds_write_b32 v5, v125 offset:12800
	ds_write_b32 v6, v126 offset:12800
	ds_write_b32 v7, v127 offset:12800
	s_or_b64 exec, exec, s[14:15]
	v_lshlrev_b32_e32 v12, 2, v12
	v_lshlrev_b32_e32 v13, 2, v13
	v_lshlrev_b32_e32 v14, 2, v14
	v_lshlrev_b32_e32 v15, 2, v15
	global_load_dword v12, v12, s[8:9]
	global_load_dword v13, v13, s[8:9]
	global_load_dword v14, v14, s[8:9]
	global_load_dword v15, v15, s[8:9]
	s_waitcnt vmcnt(0)
	v_add_u32_e32 v12, s32, v12
	v_add_u32_e32 v13, s32, v13
	v_add_u32_e32 v14, s32, v14
	v_add_u32_e32 v15, s32, v15
	v_mad_u32_u24 v120, v12, s33, v116
	v_mad_u32_u24 v121, v13, s33, v117
	v_mad_u32_u24 v122, v14, s33, v118
	v_mad_u32_u24 v123, v15, s33, v119
	global_load_dwordx4 v[16:19], v120, s[10:11]
	global_load_dwordx4 v[20:23], v116, s[16:17]
	global_load_dwordx4 v[24:27], v112, s[24:25]
	global_load_dwordx4 v[28:31], v112, s[26:27]
	global_load_dwordx4 v[32:35], v112, s[28:29]
	global_load_dwordx4 v[36:39], v112, s[30:31]
	global_load_dwordx4 v[40:43], v121, s[10:11]
	global_load_dwordx4 v[44:47], v117, s[16:17]
	global_load_dwordx4 v[48:51], v113, s[24:25]
	global_load_dwordx4 v[52:55], v113, s[26:27]
	global_load_dwordx4 v[56:59], v113, s[28:29]
	global_load_dwordx4 v[60:63], v113, s[30:31]
	global_load_dwordx4 v[64:67], v122, s[10:11]
	global_load_dwordx4 v[68:71], v118, s[16:17]
	global_load_dwordx4 v[72:75], v114, s[24:25]
	global_load_dwordx4 v[76:79], v114, s[26:27]
	global_load_dwordx4 v[80:83], v114, s[28:29]
	global_load_dwordx4 v[84:87], v114, s[30:31]
	global_load_dwordx4 v[88:91], v123, s[10:11]
	global_load_dwordx4 v[92:95], v119, s[16:17]
	global_load_dwordx4 v[96:99], v115, s[24:25]
	global_load_dwordx4 v[100:103], v115, s[26:27]
	global_load_dwordx4 v[104:107], v115, s[28:29]
	global_load_dwordx4 v[108:111], v115, s[30:31]
	s_waitcnt vmcnt(18)
	v_pk_add_f32 v[24:25], v[24:25], v[28:29]
	v_pk_add_f32 v[26:27], v[26:27], v[30:31]
	v_pk_add_f32 v[32:33], v[32:33], v[36:37]
	v_pk_add_f32 v[34:35], v[34:35], v[38:39]
	v_pk_add_f32 v[24:25], v[24:25], v[32:33]
	v_pk_add_f32 v[26:27], v[26:27], v[34:35]
	v_pk_add_f32 v[16:17], v[20:21], v[16:17]
	v_pk_add_f32 v[18:19], v[22:23], v[18:19]
	v_pk_add_f32 v[24:25], v[24:25], v[16:17]
	v_pk_add_f32 v[26:27], v[26:27], v[18:19]
	v_max_f32_e32 v24, 0, v24
	v_max_f32_e32 v25, 0, v25
	v_max_f32_e32 v26, 0, v26
	v_max_f32_e32 v27, 0, v27
	ds_write_b128 v112, v[24:27]
	s_waitcnt vmcnt(12)
	v_pk_add_f32 v[48:49], v[48:49], v[52:53]
	v_pk_add_f32 v[50:51], v[50:51], v[54:55]
	v_pk_add_f32 v[56:57], v[56:57], v[60:61]
	v_pk_add_f32 v[58:59], v[58:59], v[62:63]
	v_pk_add_f32 v[48:49], v[48:49], v[56:57]
	v_pk_add_f32 v[50:51], v[50:51], v[58:59]
	v_pk_add_f32 v[40:41], v[44:45], v[40:41]
	v_pk_add_f32 v[42:43], v[46:47], v[42:43]
	v_pk_add_f32 v[48:49], v[48:49], v[40:41]
	v_pk_add_f32 v[50:51], v[50:51], v[42:43]
	v_max_f32_e32 v48, 0, v48
	v_max_f32_e32 v49, 0, v49
	v_max_f32_e32 v50, 0, v50
	v_max_f32_e32 v51, 0, v51
	ds_write_b128 v113, v[48:51]
	s_waitcnt vmcnt(6)
	v_pk_add_f32 v[72:73], v[72:73], v[76:77]
	v_pk_add_f32 v[74:75], v[74:75], v[78:79]
	v_pk_add_f32 v[80:81], v[80:81], v[84:85]
	v_pk_add_f32 v[82:83], v[82:83], v[86:87]
	v_pk_add_f32 v[72:73], v[72:73], v[80:81]
	v_pk_add_f32 v[74:75], v[74:75], v[82:83]
	v_pk_add_f32 v[64:65], v[68:69], v[64:65]
	v_pk_add_f32 v[66:67], v[70:71], v[66:67]
	v_pk_add_f32 v[72:73], v[72:73], v[64:65]
	v_pk_add_f32 v[74:75], v[74:75], v[66:67]
	v_max_f32_e32 v72, 0, v72
	v_max_f32_e32 v73, 0, v73
	v_max_f32_e32 v74, 0, v74
	v_max_f32_e32 v75, 0, v75
	ds_write_b128 v114, v[72:75]
	s_waitcnt vmcnt(0)
	v_pk_add_f32 v[96:97], v[96:97], v[100:101]
	v_pk_add_f32 v[98:99], v[98:99], v[102:103]
	v_pk_add_f32 v[104:105], v[104:105], v[108:109]
	v_pk_add_f32 v[106:107], v[106:107], v[110:111]
	v_pk_add_f32 v[96:97], v[96:97], v[104:105]
	v_pk_add_f32 v[98:99], v[98:99], v[106:107]
	v_pk_add_f32 v[88:89], v[92:93], v[88:89]
	v_pk_add_f32 v[90:91], v[94:95], v[90:91]
	v_pk_add_f32 v[96:97], v[96:97], v[88:89]
	v_pk_add_f32 v[98:99], v[98:99], v[90:91]
	v_max_f32_e32 v96, 0, v96
	v_max_f32_e32 v97, 0, v97
	v_max_f32_e32 v98, 0, v98
	v_max_f32_e32 v99, 0, v99
	ds_write_b128 v115, v[96:99]
	s_mul_i32 s14, s6, 3
	v_cmp_gt_i32_e32 vcc, s14, v0
	s_waitcnt lgkmcnt(0)
	s_barrier
	s_and_saveexec_b64 s[2:3], vcc
	s_cbranch_execz .LBB4_17
	v_mul_u32_u24_e32 v4, s33, v130
	v_mul_u32_u24_e32 v5, s33, v131
	ds_read_b128 v[16:19], v4 offset:0
	ds_read_b128 v[36:39], v5 offset:12800
	ds_read_b128 v[20:23], v4 offset:16
	ds_read_b128 v[40:43], v5 offset:12816
	ds_read_b128 v[24:27], v4 offset:32
	ds_read_b128 v[44:47], v5 offset:12832
	ds_read_b128 v[28:31], v4 offset:48
	ds_read_b128 v[48:51], v5 offset:12848
	ds_read_b128 v[32:35], v4 offset:64
	ds_read_b128 v[52:55], v5 offset:12864
	ds_read_b128 v[56:59], v4 offset:80
	ds_read_b128 v[76:79], v5 offset:12880
	ds_read_b128 v[60:63], v4 offset:96
	ds_read_b128 v[80:83], v5 offset:12896
	ds_read_b128 v[64:67], v4 offset:112
	ds_read_b128 v[84:87], v5 offset:12912
	ds_read_b128 v[68:71], v4 offset:128
	ds_read_b128 v[88:91], v5 offset:12928
	ds_read_b128 v[72:75], v4 offset:144
	ds_read_b128 v[92:95], v5 offset:12944
	s_waitcnt lgkmcnt(10)
	v_mov_b32_e32 v139, 0
	v_fmac_f32_e32 v128, v16, v36
	v_fmac_f32_e32 v128, v17, v37
	v_fmac_f32_e32 v128, v18, v38
	v_fmac_f32_e32 v128, v19, v39
	v_fmac_f32_e32 v139, v20, v40
	v_fmac_f32_e32 v139, v21, v41
	v_fmac_f32_e32 v139, v22, v42
	v_fmac_f32_e32 v139, v23, v43
	v_fmac_f32_e32 v128, v24, v44
	v_fmac_f32_e32 v128, v25, v45
	v_fmac_f32_e32 v128, v26, v46
	v_fmac_f32_e32 v128, v27, v47
	v_fmac_f32_e32 v139, v28, v48
	v_fmac_f32_e32 v139, v29, v49
	v_fmac_f32_e32 v139, v30, v50
	v_fmac_f32_e32 v139, v31, v51
	v_fmac_f32_e32 v128, v32, v52
	v_fmac_f32_e32 v128, v33, v53
	v_fmac_f32_e32 v128, v34, v54
	v_fmac_f32_e32 v128, v35, v55
	ds_read_b128 v[16:19], v4 offset:160
	ds_read_b128 v[36:39], v5 offset:12960
	ds_read_b128 v[20:23], v4 offset:176
	ds_read_b128 v[40:43], v5 offset:12976
	ds_read_b128 v[24:27], v4 offset:192
	ds_read_b128 v[44:47], v5 offset:12992
	ds_read_b128 v[28:31], v4 offset:208
	ds_read_b128 v[48:51], v5 offset:13008
	ds_read_b128 v[32:35], v4 offset:224
	ds_read_b128 v[52:55], v5 offset:13024
	s_waitcnt lgkmcnt(10)
	v_fmac_f32_e32 v139, v56, v76
	v_fmac_f32_e32 v139, v57, v77
	v_fmac_f32_e32 v139, v58, v78
	v_fmac_f32_e32 v139, v59, v79
	v_fmac_f32_e32 v128, v60, v80
	v_fmac_f32_e32 v128, v61, v81
	v_fmac_f32_e32 v128, v62, v82
	v_fmac_f32_e32 v128, v63, v83
	v_fmac_f32_e32 v139, v64, v84
	v_fmac_f32_e32 v139, v65, v85
	v_fmac_f32_e32 v139, v66, v86
	v_fmac_f32_e32 v139, v67, v87
	v_fmac_f32_e32 v128, v68, v88
	v_fmac_f32_e32 v128, v69, v89
	v_fmac_f32_e32 v128, v70, v90
	v_fmac_f32_e32 v128, v71, v91
	v_fmac_f32_e32 v139, v72, v92
	v_fmac_f32_e32 v139, v73, v93
	v_fmac_f32_e32 v139, v74, v94
	v_fmac_f32_e32 v139, v75, v95
	ds_read_b128 v[56:59], v4 offset:240
	ds_read_b128 v[76:79], v5 offset:13040
	ds_read_b128 v[60:63], v4 offset:256
	ds_read_b128 v[80:83], v5 offset:13056
	ds_read_b128 v[64:67], v4 offset:272
	ds_read_b128 v[84:87], v5 offset:13072
	ds_read_b128 v[68:71], v4 offset:288
	ds_read_b128 v[88:91], v5 offset:13088
	ds_read_b128 v[72:75], v4 offset:304
	ds_read_b128 v[92:95], v5 offset:13104
	s_waitcnt lgkmcnt(10)
	v_fmac_f32_e32 v128, v16, v36
	v_fmac_f32_e32 v128, v17, v37
	v_fmac_f32_e32 v128, v18, v38
	v_fmac_f32_e32 v128, v19, v39
	v_fmac_f32_e32 v139, v20, v40
	v_fmac_f32_e32 v139, v21, v41
	v_fmac_f32_e32 v139, v22, v42
	v_fmac_f32_e32 v139, v23, v43
	v_fmac_f32_e32 v128, v24, v44
	v_fmac_f32_e32 v128, v25, v45
	v_fmac_f32_e32 v128, v26, v46
	v_fmac_f32_e32 v128, v27, v47
	v_fmac_f32_e32 v139, v28, v48
	v_fmac_f32_e32 v139, v29, v49
	v_fmac_f32_e32 v139, v30, v50
	v_fmac_f32_e32 v139, v31, v51
	v_fmac_f32_e32 v128, v32, v52
	v_fmac_f32_e32 v128, v33, v53
	v_fmac_f32_e32 v128, v34, v54
	v_fmac_f32_e32 v128, v35, v55
	ds_read_b128 v[16:19], v4 offset:320
	ds_read_b128 v[36:39], v5 offset:13120
	ds_read_b128 v[20:23], v4 offset:336
	ds_read_b128 v[40:43], v5 offset:13136
	ds_read_b128 v[24:27], v4 offset:352
	ds_read_b128 v[44:47], v5 offset:13152
	ds_read_b128 v[28:31], v4 offset:368
	ds_read_b128 v[48:51], v5 offset:13168
	ds_read_b128 v[32:35], v4 offset:384
	ds_read_b128 v[52:55], v5 offset:13184
	s_waitcnt lgkmcnt(10)
	v_fmac_f32_e32 v139, v56, v76
	v_fmac_f32_e32 v139, v57, v77
	v_fmac_f32_e32 v139, v58, v78
	v_fmac_f32_e32 v139, v59, v79
	v_fmac_f32_e32 v128, v60, v80
	v_fmac_f32_e32 v128, v61, v81
	v_fmac_f32_e32 v128, v62, v82
	v_fmac_f32_e32 v128, v63, v83
	v_fmac_f32_e32 v139, v64, v84
	v_fmac_f32_e32 v139, v65, v85
	v_fmac_f32_e32 v139, v66, v86
	v_fmac_f32_e32 v139, v67, v87
	v_fmac_f32_e32 v128, v68, v88
	v_fmac_f32_e32 v128, v69, v89
	v_fmac_f32_e32 v128, v70, v90
	v_fmac_f32_e32 v128, v71, v91
	v_fmac_f32_e32 v139, v72, v92
	v_fmac_f32_e32 v139, v73, v93
	v_fmac_f32_e32 v139, v74, v94
	v_fmac_f32_e32 v139, v75, v95
	s_waitcnt lgkmcnt(0)
	v_fmac_f32_e32 v128, v16, v36
	v_fmac_f32_e32 v128, v17, v37
	v_fmac_f32_e32 v128, v18, v38
	v_fmac_f32_e32 v128, v19, v39
	v_fmac_f32_e32 v139, v20, v40
	v_fmac_f32_e32 v139, v21, v41
	v_fmac_f32_e32 v139, v22, v42
	v_fmac_f32_e32 v139, v23, v43
	v_fmac_f32_e32 v128, v24, v44
	v_fmac_f32_e32 v128, v25, v45
	v_fmac_f32_e32 v128, v26, v46
	v_fmac_f32_e32 v128, v27, v47
	v_fmac_f32_e32 v139, v28, v48
	v_fmac_f32_e32 v139, v29, v49
	v_fmac_f32_e32 v139, v30, v50
	v_fmac_f32_e32 v139, v31, v51
	v_fmac_f32_e32 v128, v32, v52
	v_fmac_f32_e32 v128, v33, v53
	v_fmac_f32_e32 v128, v34, v54
	v_fmac_f32_e32 v128, v35, v55
	v_add_f32_e32 v128, v128, v139
	v_mul_u32_u24_e32 v6, 3, v129
	v_add_lshl_u32 v6, v6, v131, 2
	global_store_dword v6, v128, s[40:41]
